# merge / MoBA-merge output stores back to the default cache policy (write-through no longer needed once the loop waits stopped draining them)
# speedup vs baseline: 1.0037x; 1.0030x over previous
.Lmg1_w:
	s_waitcnt vmcnt(14)
	s_mov_b32 s50, 1
	v_max3_f32 v8, v32, v33, v34
	v_sub_f32_e32 v9, v32, v8
	v_mul_f32_e32 v13, 0x3fb8aa3b, v9
	v_fma_f32 v14, v9, s94, -v13
	v_rndne_f32_e32 v15, v13
	v_fmac_f32_e32 v14, 0x32a5705f, v9
	v_sub_f32_e32 v13, v13, v15
	v_add_f32_e32 v13, v13, v14
	v_exp_f32_e32 v10, v13
	v_cvt_i32_f32_e32 v15, v15
	v_cmp_ngt_f32_e32 vcc, s95, v9
	v_ldexp_f32 v10, v10, v15
	s_nop 1
	v_cndmask_b32_e32 v10, 0, v10, vcc
	v_cmp_nlt_f32_e32 vcc, s96, v9
	s_nop 1
	v_cndmask_b32_e32 v10, v227, v10, vcc
	v_sub_f32_e32 v9, v33, v8
	v_mul_f32_e32 v13, 0x3fb8aa3b, v9
	v_fma_f32 v14, v9, s94, -v13
	v_rndne_f32_e32 v15, v13
	v_fmac_f32_e32 v14, 0x32a5705f, v9
	v_sub_f32_e32 v13, v13, v15
	v_add_f32_e32 v13, v13, v14
	v_exp_f32_e32 v11, v13
	v_cvt_i32_f32_e32 v15, v15
	v_cmp_ngt_f32_e32 vcc, s95, v9
	v_ldexp_f32 v11, v11, v15
	s_nop 1
	v_cndmask_b32_e32 v11, 0, v11, vcc
	v_cmp_nlt_f32_e32 vcc, s96, v9
	s_nop 1
	v_cndmask_b32_e32 v11, v227, v11, vcc
	v_sub_f32_e32 v9, v34, v8
	v_mul_f32_e32 v13, 0x3fb8aa3b, v9
	v_fma_f32 v14, v9, s94, -v13
	v_rndne_f32_e32 v15, v13
	v_fmac_f32_e32 v14, 0x32a5705f, v9
	v_sub_f32_e32 v13, v13, v15
	v_add_f32_e32 v13, v13, v14
	v_exp_f32_e32 v12, v13
	v_cvt_i32_f32_e32 v15, v15
	v_cmp_ngt_f32_e32 vcc, s95, v9
	v_ldexp_f32 v12, v12, v15
	s_nop 1
	v_cndmask_b32_e32 v12, 0, v12, vcc
	v_cmp_nlt_f32_e32 vcc, s96, v9
	s_nop 1
	v_cndmask_b32_e32 v12, v227, v12, vcc
	v_add_f32_e32 v16, v10, v11
	v_add_f32_e32 v16, v12, v16
	v_div_scale_f32 v17, s[2:3], v16, v16, 1.0
	v_rcp_f32_e32 v18, v17
	s_nop 0
	v_fma_f32 v19, -v17, v18, 1.0
	v_fmac_f32_e32 v18, v19, v18
	v_div_scale_f32 v20, vcc, 1.0, v16, 1.0
	v_mul_f32_e32 v21, v20, v18
	v_fma_f32 v22, -v17, v21, v20
	v_fmac_f32_e32 v21, v22, v18
	v_fma_f32 v17, -v17, v21, v20
	v_div_fmas_f32 v17, v17, v18, v21
	v_div_fixup_f32 v16, v17, v16, 1.0
	v_mul_f32_e32 v16, 0x41800000, v16
	v_mul_f32_e32 v10, v10, v16
	v_mul_f32_e32 v11, v11, v16
	v_mul_f32_e32 v12, v12, v16
	v_lshlrev_b32_e32 v13, 16, v36
	v_and_b32_e32 v14, 0xffff0000, v36
	v_mul_f32_e32 v20, v10, v13
	v_mul_f32_e32 v21, v10, v14
	v_lshlrev_b32_e32 v13, 16, v40
	v_and_b32_e32 v14, 0xffff0000, v40
	v_fmac_f32_e32 v20, v11, v13
	v_fmac_f32_e32 v21, v11, v14
	v_lshlrev_b32_e32 v13, 16, v44
	v_and_b32_e32 v14, 0xffff0000, v44
	v_fmac_f32_e32 v20, v12, v13
	v_fmac_f32_e32 v21, v12, v14
	v_lshlrev_b32_e32 v13, 16, v37
	v_and_b32_e32 v14, 0xffff0000, v37
	v_mul_f32_e32 v22, v10, v13
	v_mul_f32_e32 v23, v10, v14
	v_lshlrev_b32_e32 v13, 16, v41
	v_and_b32_e32 v14, 0xffff0000, v41
	v_fmac_f32_e32 v22, v11, v13
	v_fmac_f32_e32 v23, v11, v14
	v_lshlrev_b32_e32 v13, 16, v45
	v_and_b32_e32 v14, 0xffff0000, v45
	v_fmac_f32_e32 v22, v12, v13
	v_fmac_f32_e32 v23, v12, v14
	v_lshlrev_b32_e32 v13, 16, v38
	v_and_b32_e32 v14, 0xffff0000, v38
	v_mul_f32_e32 v24, v10, v13
	v_mul_f32_e32 v25, v10, v14
	v_lshlrev_b32_e32 v13, 16, v42
	v_and_b32_e32 v14, 0xffff0000, v42
	v_fmac_f32_e32 v24, v11, v13
	v_fmac_f32_e32 v25, v11, v14
	v_lshlrev_b32_e32 v13, 16, v46
	v_and_b32_e32 v14, 0xffff0000, v46
	v_fmac_f32_e32 v24, v12, v13
	v_fmac_f32_e32 v25, v12, v14
	v_lshlrev_b32_e32 v13, 16, v39
	v_and_b32_e32 v14, 0xffff0000, v39
	v_mul_f32_e32 v26, v10, v13
	v_mul_f32_e32 v27, v10, v14
	v_lshlrev_b32_e32 v13, 16, v43
	v_and_b32_e32 v14, 0xffff0000, v43
	v_fmac_f32_e32 v26, v11, v13
	v_fmac_f32_e32 v27, v11, v14
	v_lshlrev_b32_e32 v13, 16, v47
	v_and_b32_e32 v14, 0xffff0000, v47
	v_fmac_f32_e32 v26, v12, v13
	v_fmac_f32_e32 v27, v12, v14
	v_mov_b32_e32 v16, 0
	v_mov_b32_e32 v17, 0
	v_lshlrev_b32_e32 v7, 3, v35
	v_cvt_pk_fp8_f32 v16, v20, v21
	v_cvt_pk_fp8_f32 v17, v24, v25
	s_nop 0
	v_cvt_pk_fp8_f32 v16, v22, v23 op_sel:[0,0,1]
	v_cvt_pk_fp8_f32 v17, v26, v27 op_sel:[0,0,1]
	s_nop 0
	global_store_dwordx2 v7, v[16:17], s[30:31]
	v_max3_f32 v8, v48, v49, v50
	v_sub_f32_e32 v9, v48, v8
	v_mul_f32_e32 v13, 0x3fb8aa3b, v9
	v_fma_f32 v14, v9, s94, -v13
	v_rndne_f32_e32 v15, v13
	v_fmac_f32_e32 v14, 0x32a5705f, v9
	v_sub_f32_e32 v13, v13, v15
	v_add_f32_e32 v13, v13, v14
	v_exp_f32_e32 v10, v13
	v_cvt_i32_f32_e32 v15, v15
	v_cmp_ngt_f32_e32 vcc, s95, v9
	v_ldexp_f32 v10, v10, v15
	s_nop 1
	v_cndmask_b32_e32 v10, 0, v10, vcc
	v_cmp_nlt_f32_e32 vcc, s96, v9
	s_nop 1
	v_cndmask_b32_e32 v10, v227, v10, vcc
	v_sub_f32_e32 v9, v49, v8
	v_mul_f32_e32 v13, 0x3fb8aa3b, v9
	v_fma_f32 v14, v9, s94, -v13
	v_rndne_f32_e32 v15, v13
	v_fmac_f32_e32 v14, 0x32a5705f, v9
	v_sub_f32_e32 v13, v13, v15
	v_add_f32_e32 v13, v13, v14
	v_exp_f32_e32 v11, v13
	v_cvt_i32_f32_e32 v15, v15
	v_cmp_ngt_f32_e32 vcc, s95, v9
	v_ldexp_f32 v11, v11, v15
	s_nop 1
	v_cndmask_b32_e32 v11, 0, v11, vcc
	v_cmp_nlt_f32_e32 vcc, s96, v9
	s_nop 1
	v_cndmask_b32_e32 v11, v227, v11, vcc
	v_sub_f32_e32 v9, v50, v8
	v_mul_f32_e32 v13, 0x3fb8aa3b, v9
	v_fma_f32 v14, v9, s94, -v13
	v_rndne_f32_e32 v15, v13
	v_fmac_f32_e32 v14, 0x32a5705f, v9
	v_sub_f32_e32 v13, v13, v15
	v_add_f32_e32 v13, v13, v14
	v_exp_f32_e32 v12, v13
	v_cvt_i32_f32_e32 v15, v15
	v_cmp_ngt_f32_e32 vcc, s95, v9
	v_ldexp_f32 v12, v12, v15
	s_nop 1
	v_cndmask_b32_e32 v12, 0, v12, vcc
	v_cmp_nlt_f32_e32 vcc, s96, v9
	s_nop 1
	v_cndmask_b32_e32 v12, v227, v12, vcc
	v_add_f32_e32 v16, v10, v11
	v_add_f32_e32 v16, v12, v16
	v_div_scale_f32 v17, s[2:3], v16, v16, 1.0
	v_rcp_f32_e32 v18, v17
	s_nop 0
	v_fma_f32 v19, -v17, v18, 1.0
	v_fmac_f32_e32 v18, v19, v18
	v_div_scale_f32 v20, vcc, 1.0, v16, 1.0
	v_mul_f32_e32 v21, v20, v18
	v_fma_f32 v22, -v17, v21, v20
	v_fmac_f32_e32 v21, v22, v18
	v_fma_f32 v17, -v17, v21, v20
	v_div_fmas_f32 v17, v17, v18, v21
	v_div_fixup_f32 v16, v17, v16, 1.0
	v_mul_f32_e32 v16, 0x41800000, v16
	v_mul_f32_e32 v10, v10, v16
	v_mul_f32_e32 v11, v11, v16
	v_mul_f32_e32 v12, v12, v16
	v_lshlrev_b32_e32 v13, 16, v52
	v_and_b32_e32 v14, 0xffff0000, v52
	v_mul_f32_e32 v20, v10, v13
	v_mul_f32_e32 v21, v10, v14
	v_lshlrev_b32_e32 v13, 16, v56
	v_and_b32_e32 v14, 0xffff0000, v56
	v_fmac_f32_e32 v20, v11, v13
	v_fmac_f32_e32 v21, v11, v14
	v_lshlrev_b32_e32 v13, 16, v60
	v_and_b32_e32 v14, 0xffff0000, v60
	v_fmac_f32_e32 v20, v12, v13
	v_fmac_f32_e32 v21, v12, v14
	v_lshlrev_b32_e32 v13, 16, v53
	v_and_b32_e32 v14, 0xffff0000, v53
	v_mul_f32_e32 v22, v10, v13
	v_mul_f32_e32 v23, v10, v14
	v_lshlrev_b32_e32 v13, 16, v57
	v_and_b32_e32 v14, 0xffff0000, v57
	v_fmac_f32_e32 v22, v11, v13
	v_fmac_f32_e32 v23, v11, v14
	v_lshlrev_b32_e32 v13, 16, v61
	v_and_b32_e32 v14, 0xffff0000, v61
	v_fmac_f32_e32 v22, v12, v13
	v_fmac_f32_e32 v23, v12, v14
	v_lshlrev_b32_e32 v13, 16, v54
	v_and_b32_e32 v14, 0xffff0000, v54
	v_mul_f32_e32 v24, v10, v13
	v_mul_f32_e32 v25, v10, v14
	v_lshlrev_b32_e32 v13, 16, v58
	v_and_b32_e32 v14, 0xffff0000, v58
	v_fmac_f32_e32 v24, v11, v13
	v_fmac_f32_e32 v25, v11, v14
	v_lshlrev_b32_e32 v13, 16, v62
	v_and_b32_e32 v14, 0xffff0000, v62
	v_fmac_f32_e32 v24, v12, v13
	v_fmac_f32_e32 v25, v12, v14
	v_lshlrev_b32_e32 v13, 16, v55
	v_and_b32_e32 v14, 0xffff0000, v55
	v_mul_f32_e32 v26, v10, v13
	v_mul_f32_e32 v27, v10, v14
	v_lshlrev_b32_e32 v13, 16, v59
	v_and_b32_e32 v14, 0xffff0000, v59
	v_fmac_f32_e32 v26, v11, v13
	v_fmac_f32_e32 v27, v11, v14
	v_lshlrev_b32_e32 v13, 16, v63
	v_and_b32_e32 v14, 0xffff0000, v63
	v_fmac_f32_e32 v26, v12, v13
	v_fmac_f32_e32 v27, v12, v14
	v_mov_b32_e32 v16, 0
	v_mov_b32_e32 v17, 0
	v_lshlrev_b32_e32 v7, 3, v51
	v_cvt_pk_fp8_f32 v16, v20, v21
	v_cvt_pk_fp8_f32 v17, v24, v25
	s_nop 0
	v_cvt_pk_fp8_f32 v16, v22, v23 op_sel:[0,0,1]
	v_cvt_pk_fp8_f32 v17, v26, v27 op_sel:[0,0,1]
	s_nop 0
	global_store_dwordx2 v7, v[16:17], s[30:31]
	v_add_u32_e32 v2, s47, v2
	s_add_u32 s44, s44, s47
	v_min_u32_e32 v35, s43, v2
	v_lshrrev_b32_e32 v6, 1, v35
	v_lshlrev_b32_e32 v7, 4, v35
	v_and_b32_e32 v6, -4, v6
	global_load_dwordx4 v[36:39], v7, s[14:15]
	global_load_dwordx4 v[40:43], v7, s[16:17]
	global_load_dwordx4 v[44:47], v7, s[18:19]
	global_load_dword v32, v6, s[12:13]
	global_load_dword v33, v6, s[38:39]
	global_load_dword v34, v6, s[40:41]
	v_add_u32_e32 v51, s42, v2
	v_min_u32_e32 v51, s43, v51
	v_lshrrev_b32_e32 v6, 1, v51
	v_lshlrev_b32_e32 v7, 4, v51
	v_and_b32_e32 v6, -4, v6
	global_load_dwordx4 v[52:55], v7, s[14:15]
	global_load_dwordx4 v[56:59], v7, s[16:17]
	global_load_dwordx4 v[60:63], v7, s[18:19]
	global_load_dword v48, v6, s[12:13]
	global_load_dword v49, v6, s[38:39]
	global_load_dword v50, v6, s[40:41]
	s_waitcnt vmcnt(14)
	v_max3_f32 v8, v190, v191, v192
	v_sub_f32_e32 v9, v190, v8
	v_mul_f32_e32 v13, 0x3fb8aa3b, v9
	v_fma_f32 v14, v9, s94, -v13
	v_rndne_f32_e32 v15, v13
	v_fmac_f32_e32 v14, 0x32a5705f, v9
	v_sub_f32_e32 v13, v13, v15
	v_add_f32_e32 v13, v13, v14
	v_exp_f32_e32 v10, v13
	v_cvt_i32_f32_e32 v15, v15
	v_cmp_ngt_f32_e32 vcc, s95, v9
	v_ldexp_f32 v10, v10, v15
	s_nop 1
	v_cndmask_b32_e32 v10, 0, v10, vcc
	v_cmp_nlt_f32_e32 vcc, s96, v9
	s_nop 1
	v_cndmask_b32_e32 v10, v227, v10, vcc
	v_sub_f32_e32 v9, v191, v8
	v_mul_f32_e32 v13, 0x3fb8aa3b, v9
	v_fma_f32 v14, v9, s94, -v13
	v_rndne_f32_e32 v15, v13
	v_fmac_f32_e32 v14, 0x32a5705f, v9
	v_sub_f32_e32 v13, v13, v15
	v_add_f32_e32 v13, v13, v14
	v_exp_f32_e32 v11, v13
	v_cvt_i32_f32_e32 v15, v15
	v_cmp_ngt_f32_e32 vcc, s95, v9
	v_ldexp_f32 v11, v11, v15
	s_nop 1
	v_cndmask_b32_e32 v11, 0, v11, vcc
	v_cmp_nlt_f32_e32 vcc, s96, v9
	s_nop 1
	v_cndmask_b32_e32 v11, v227, v11, vcc
	v_sub_f32_e32 v9, v192, v8
	v_mul_f32_e32 v13, 0x3fb8aa3b, v9
	v_fma_f32 v14, v9, s94, -v13
	v_rndne_f32_e32 v15, v13
	v_fmac_f32_e32 v14, 0x32a5705f, v9
	v_sub_f32_e32 v13, v13, v15
	v_add_f32_e32 v13, v13, v14
	v_exp_f32_e32 v12, v13
	v_cvt_i32_f32_e32 v15, v15
	v_cmp_ngt_f32_e32 vcc, s95, v9
	v_ldexp_f32 v12, v12, v15
	s_nop 1
	v_cndmask_b32_e32 v12, 0, v12, vcc
	v_cmp_nlt_f32_e32 vcc, s96, v9
	s_nop 1
	v_cndmask_b32_e32 v12, v227, v12, vcc
	v_add_f32_e32 v16, v10, v11
	v_add_f32_e32 v16, v12, v16
	v_div_scale_f32 v17, s[2:3], v16, v16, 1.0
	v_rcp_f32_e32 v18, v17
	s_nop 0
	v_fma_f32 v19, -v17, v18, 1.0
	v_fmac_f32_e32 v18, v19, v18
	v_div_scale_f32 v20, vcc, 1.0, v16, 1.0
	v_mul_f32_e32 v21, v20, v18
	v_fma_f32 v22, -v17, v21, v20
	v_fmac_f32_e32 v21, v22, v18
	v_fma_f32 v17, -v17, v21, v20
	v_div_fmas_f32 v17, v17, v18, v21
	v_div_fixup_f32 v16, v17, v16, 1.0
	v_mul_f32_e32 v16, 0x41800000, v16
	v_mul_f32_e32 v10, v10, v16
	v_mul_f32_e32 v11, v11, v16
	v_mul_f32_e32 v12, v12, v16
	v_lshlrev_b32_e32 v13, 16, v194
	v_and_b32_e32 v14, 0xffff0000, v194
	v_mul_f32_e32 v20, v10, v13
	v_mul_f32_e32 v21, v10, v14
	v_lshlrev_b32_e32 v13, 16, v198
	v_and_b32_e32 v14, 0xffff0000, v198
	v_fmac_f32_e32 v20, v11, v13
	v_fmac_f32_e32 v21, v11, v14
	v_lshlrev_b32_e32 v13, 16, v202
	v_and_b32_e32 v14, 0xffff0000, v202
	v_fmac_f32_e32 v20, v12, v13
	v_fmac_f32_e32 v21, v12, v14
	v_lshlrev_b32_e32 v13, 16, v195
	v_and_b32_e32 v14, 0xffff0000, v195
	v_mul_f32_e32 v22, v10, v13
	v_mul_f32_e32 v23, v10, v14
	v_lshlrev_b32_e32 v13, 16, v199
	v_and_b32_e32 v14, 0xffff0000, v199
	v_fmac_f32_e32 v22, v11, v13
	v_fmac_f32_e32 v23, v11, v14
	v_lshlrev_b32_e32 v13, 16, v203
	v_and_b32_e32 v14, 0xffff0000, v203
	v_fmac_f32_e32 v22, v12, v13
	v_fmac_f32_e32 v23, v12, v14
	v_lshlrev_b32_e32 v13, 16, v196
	v_and_b32_e32 v14, 0xffff0000, v196
	v_mul_f32_e32 v24, v10, v13
	v_mul_f32_e32 v25, v10, v14
	v_lshlrev_b32_e32 v13, 16, v200
	v_and_b32_e32 v14, 0xffff0000, v200
	v_fmac_f32_e32 v24, v11, v13
	v_fmac_f32_e32 v25, v11, v14
	v_lshlrev_b32_e32 v13, 16, v204
	v_and_b32_e32 v14, 0xffff0000, v204
	v_fmac_f32_e32 v24, v12, v13
	v_fmac_f32_e32 v25, v12, v14
	v_lshlrev_b32_e32 v13, 16, v197
	v_and_b32_e32 v14, 0xffff0000, v197
	v_mul_f32_e32 v26, v10, v13
	v_mul_f32_e32 v27, v10, v14
	v_lshlrev_b32_e32 v13, 16, v201
	v_and_b32_e32 v14, 0xffff0000, v201
	v_fmac_f32_e32 v26, v11, v13
	v_fmac_f32_e32 v27, v11, v14
	v_lshlrev_b32_e32 v13, 16, v205
	v_and_b32_e32 v14, 0xffff0000, v205
	v_fmac_f32_e32 v26, v12, v13
	v_fmac_f32_e32 v27, v12, v14
	v_mov_b32_e32 v16, 0
	v_mov_b32_e32 v17, 0
	v_lshlrev_b32_e32 v7, 3, v193
	v_cvt_pk_fp8_f32 v16, v20, v21
	v_cvt_pk_fp8_f32 v17, v24, v25
	s_nop 0
	v_cvt_pk_fp8_f32 v16, v22, v23 op_sel:[0,0,1]
	v_cvt_pk_fp8_f32 v17, v26, v27 op_sel:[0,0,1]
	s_nop 0
	global_store_dwordx2 v7, v[16:17], s[30:31]
	v_max3_f32 v8, v206, v207, v208
	v_sub_f32_e32 v9, v206, v8
	v_mul_f32_e32 v13, 0x3fb8aa3b, v9
	v_fma_f32 v14, v9, s94, -v13
	v_rndne_f32_e32 v15, v13
	v_fmac_f32_e32 v14, 0x32a5705f, v9
	v_sub_f32_e32 v13, v13, v15
	v_add_f32_e32 v13, v13, v14
	v_exp_f32_e32 v10, v13
	v_cvt_i32_f32_e32 v15, v15
	v_cmp_ngt_f32_e32 vcc, s95, v9
	v_ldexp_f32 v10, v10, v15
	s_nop 1
	v_cndmask_b32_e32 v10, 0, v10, vcc
	v_cmp_nlt_f32_e32 vcc, s96, v9
	s_nop 1
	v_cndmask_b32_e32 v10, v227, v10, vcc
	v_sub_f32_e32 v9, v207, v8
	v_mul_f32_e32 v13, 0x3fb8aa3b, v9
	v_fma_f32 v14, v9, s94, -v13
	v_rndne_f32_e32 v15, v13
	v_fmac_f32_e32 v14, 0x32a5705f, v9
	v_sub_f32_e32 v13, v13, v15
	v_add_f32_e32 v13, v13, v14
	v_exp_f32_e32 v11, v13
	v_cvt_i32_f32_e32 v15, v15
	v_cmp_ngt_f32_e32 vcc, s95, v9
	v_ldexp_f32 v11, v11, v15
	s_nop 1
	v_cndmask_b32_e32 v11, 0, v11, vcc
	v_cmp_nlt_f32_e32 vcc, s96, v9
	s_nop 1
	v_cndmask_b32_e32 v11, v227, v11, vcc
	v_sub_f32_e32 v9, v208, v8
	v_mul_f32_e32 v13, 0x3fb8aa3b, v9
	v_fma_f32 v14, v9, s94, -v13
	v_rndne_f32_e32 v15, v13
	v_fmac_f32_e32 v14, 0x32a5705f, v9
	v_sub_f32_e32 v13, v13, v15
	v_add_f32_e32 v13, v13, v14
	v_exp_f32_e32 v12, v13
	v_cvt_i32_f32_e32 v15, v15
	v_cmp_ngt_f32_e32 vcc, s95, v9
	v_ldexp_f32 v12, v12, v15
	s_nop 1
	v_cndmask_b32_e32 v12, 0, v12, vcc
	v_cmp_nlt_f32_e32 vcc, s96, v9
	s_nop 1
	v_cndmask_b32_e32 v12, v227, v12, vcc
	v_add_f32_e32 v16, v10, v11
	v_add_f32_e32 v16, v12, v16
	v_div_scale_f32 v17, s[2:3], v16, v16, 1.0
	v_rcp_f32_e32 v18, v17
	s_nop 0
	v_fma_f32 v19, -v17, v18, 1.0
	v_fmac_f32_e32 v18, v19, v18
	v_div_scale_f32 v20, vcc, 1.0, v16, 1.0
	v_mul_f32_e32 v21, v20, v18
	v_fma_f32 v22, -v17, v21, v20
	v_fmac_f32_e32 v21, v22, v18
	v_fma_f32 v17, -v17, v21, v20
	v_div_fmas_f32 v17, v17, v18, v21
	v_div_fixup_f32 v16, v17, v16, 1.0
	v_mul_f32_e32 v16, 0x41800000, v16
	v_mul_f32_e32 v10, v10, v16
	v_mul_f32_e32 v11, v11, v16
	v_mul_f32_e32 v12, v12, v16
	v_lshlrev_b32_e32 v13, 16, v210
	v_and_b32_e32 v14, 0xffff0000, v210
	v_mul_f32_e32 v20, v10, v13
	v_mul_f32_e32 v21, v10, v14
	v_lshlrev_b32_e32 v13, 16, v214
	v_and_b32_e32 v14, 0xffff0000, v214
	v_fmac_f32_e32 v20, v11, v13
	v_fmac_f32_e32 v21, v11, v14
	v_lshlrev_b32_e32 v13, 16, v238
	v_and_b32_e32 v14, 0xffff0000, v238
	v_fmac_f32_e32 v20, v12, v13
	v_fmac_f32_e32 v21, v12, v14
	v_lshlrev_b32_e32 v13, 16, v211
	v_and_b32_e32 v14, 0xffff0000, v211
	v_mul_f32_e32 v22, v10, v13
	v_mul_f32_e32 v23, v10, v14
	v_lshlrev_b32_e32 v13, 16, v215
	v_and_b32_e32 v14, 0xffff0000, v215
	v_fmac_f32_e32 v22, v11, v13
	v_fmac_f32_e32 v23, v11, v14
	v_lshlrev_b32_e32 v13, 16, v239
	v_and_b32_e32 v14, 0xffff0000, v239
	v_fmac_f32_e32 v22, v12, v13
	v_fmac_f32_e32 v23, v12, v14
	v_lshlrev_b32_e32 v13, 16, v212
	v_and_b32_e32 v14, 0xffff0000, v212
	v_mul_f32_e32 v24, v10, v13
	v_mul_f32_e32 v25, v10, v14
	v_lshlrev_b32_e32 v13, 16, v216
	v_and_b32_e32 v14, 0xffff0000, v216
	v_fmac_f32_e32 v24, v11, v13
	v_fmac_f32_e32 v25, v11, v14
	v_lshlrev_b32_e32 v13, 16, v240
	v_and_b32_e32 v14, 0xffff0000, v240
	v_fmac_f32_e32 v24, v12, v13
	v_fmac_f32_e32 v25, v12, v14
	v_lshlrev_b32_e32 v13, 16, v213
	v_and_b32_e32 v14, 0xffff0000, v213
	v_mul_f32_e32 v26, v10, v13
	v_mul_f32_e32 v27, v10, v14
	v_lshlrev_b32_e32 v13, 16, v217
	v_and_b32_e32 v14, 0xffff0000, v217
	v_fmac_f32_e32 v26, v11, v13
	v_fmac_f32_e32 v27, v11, v14
	v_lshlrev_b32_e32 v13, 16, v241
	v_and_b32_e32 v14, 0xffff0000, v241
	v_fmac_f32_e32 v26, v12, v13
	v_fmac_f32_e32 v27, v12, v14
	v_mov_b32_e32 v16, 0
	v_mov_b32_e32 v17, 0
	v_lshlrev_b32_e32 v7, 3, v209
	v_cvt_pk_fp8_f32 v16, v20, v21
	v_cvt_pk_fp8_f32 v17, v24, v25
	s_nop 0
	v_cvt_pk_fp8_f32 v16, v22, v23 op_sel:[0,0,1]
	v_cvt_pk_fp8_f32 v17, v26, v27 op_sel:[0,0,1]
	s_nop 0
	global_store_dwordx2 v7, v[16:17], s[30:31]
	s_cmp_le_u32 s44, s43
	s_cbranch_scc1 .Lmg1_loop

.Lmbm_w:
	s_waitcnt vmcnt(12)
	s_mov_b32 s50, 1
	v_bfe_u32 v8, v190, 15, 5
	v_cmp_lt_u32_e32 vcc, 0, v8
	s_nop 1
	v_cndmask_b32_e32 v32, v149, v32, vcc
	v_cmp_lt_u32_e32 vcc, 1, v8
	s_nop 1
	v_cndmask_b32_e32 v33, v149, v33, vcc
	v_cmp_lt_u32_e32 vcc, 2, v8
	s_nop 1
	v_cndmask_b32_e32 v34, v149, v34, vcc
	v_max3_f32 v9, v32, v33, v34
	v_max_f32_e32 v9, v9, v35
	v_sub_f32_e32 v10, v32, v9
	v_mul_f32_e32 v16, 0x3fb8aa3b, v10
	v_fma_f32 v17, v10, s94, -v16
	v_rndne_f32_e32 v18, v16
	v_fmac_f32_e32 v17, 0x32a5705f, v10
	v_sub_f32_e32 v16, v16, v18
	v_add_f32_e32 v16, v16, v17
	v_exp_f32_e32 v12, v16
	v_cvt_i32_f32_e32 v18, v18
	v_cmp_ngt_f32_e32 vcc, s95, v10
	v_ldexp_f32 v12, v12, v18
	s_nop 1
	v_cndmask_b32_e32 v12, 0, v12, vcc
	v_cmp_nlt_f32_e32 vcc, s96, v10
	s_nop 1
	v_cndmask_b32_e32 v12, v227, v12, vcc
	v_sub_f32_e32 v10, v33, v9
	v_mul_f32_e32 v16, 0x3fb8aa3b, v10
	v_fma_f32 v17, v10, s94, -v16
	v_rndne_f32_e32 v18, v16
	v_fmac_f32_e32 v17, 0x32a5705f, v10
	v_sub_f32_e32 v16, v16, v18
	v_add_f32_e32 v16, v16, v17
	v_exp_f32_e32 v13, v16
	v_cvt_i32_f32_e32 v18, v18
	v_cmp_ngt_f32_e32 vcc, s95, v10
	v_ldexp_f32 v13, v13, v18
	s_nop 1
	v_cndmask_b32_e32 v13, 0, v13, vcc
	v_cmp_nlt_f32_e32 vcc, s96, v10
	s_nop 1
	v_cndmask_b32_e32 v13, v227, v13, vcc
	v_sub_f32_e32 v10, v34, v9
	v_mul_f32_e32 v16, 0x3fb8aa3b, v10
	v_fma_f32 v17, v10, s94, -v16
	v_rndne_f32_e32 v18, v16
	v_fmac_f32_e32 v17, 0x32a5705f, v10
	v_sub_f32_e32 v16, v16, v18
	v_add_f32_e32 v16, v16, v17
	v_exp_f32_e32 v14, v16
	v_cvt_i32_f32_e32 v18, v18
	v_cmp_ngt_f32_e32 vcc, s95, v10
	v_ldexp_f32 v14, v14, v18
	s_nop 1
	v_cndmask_b32_e32 v14, 0, v14, vcc
	v_cmp_nlt_f32_e32 vcc, s96, v10
	s_nop 1
	v_cndmask_b32_e32 v14, v227, v14, vcc
	v_sub_f32_e32 v10, v35, v9
	v_mul_f32_e32 v16, 0x3fb8aa3b, v10
	v_fma_f32 v17, v10, s94, -v16
	v_rndne_f32_e32 v18, v16
	v_fmac_f32_e32 v17, 0x32a5705f, v10
	v_sub_f32_e32 v16, v16, v18
	v_add_f32_e32 v16, v16, v17
	v_exp_f32_e32 v15, v16
	v_cvt_i32_f32_e32 v18, v18
	v_cmp_ngt_f32_e32 vcc, s95, v10
	v_ldexp_f32 v15, v15, v18
	s_nop 1
	v_cndmask_b32_e32 v15, 0, v15, vcc
	v_cmp_nlt_f32_e32 vcc, s96, v10
	s_nop 1
	v_cndmask_b32_e32 v15, v227, v15, vcc
	v_add_f32_e32 v16, v12, v13
	v_add_f32_e32 v16, v14, v16
	v_add_f32_e32 v16, v15, v16
	v_div_scale_f32 v17, s[2:3], v16, v16, 1.0
	v_rcp_f32_e32 v18, v17
	s_nop 0
	v_fma_f32 v19, -v17, v18, 1.0
	v_fmac_f32_e32 v18, v19, v18
	v_div_scale_f32 v20, vcc, 1.0, v16, 1.0
	v_mul_f32_e32 v21, v20, v18
	v_fma_f32 v22, -v17, v21, v20
	v_fmac_f32_e32 v21, v22, v18
	v_fma_f32 v17, -v17, v21, v20
	v_div_fmas_f32 v17, v17, v18, v21
	v_div_fixup_f32 v16, v17, v16, 1.0
	v_mul_f32_e32 v16, 0x41800000, v16
	v_mul_f32_e32 v12, v12, v16
	v_mul_f32_e32 v13, v13, v16
	v_mul_f32_e32 v14, v14, v16
	v_mul_f32_e32 v15, v15, v16
	v_lshlrev_b32_e32 v16, 16, v36
	v_and_b32_e32 v17, 0xffff0000, v36
	v_mul_f32_e32 v20, v12, v16
	v_mul_f32_e32 v21, v12, v17
	v_lshlrev_b32_e32 v16, 16, v40
	v_and_b32_e32 v17, 0xffff0000, v40
	v_fmac_f32_e32 v20, v13, v16
	v_fmac_f32_e32 v21, v13, v17
	v_lshlrev_b32_e32 v16, 16, v44
	v_and_b32_e32 v17, 0xffff0000, v44
	v_fmac_f32_e32 v20, v14, v16
	v_fmac_f32_e32 v21, v14, v17
	v_lshlrev_b32_e32 v16, 16, v48
	v_and_b32_e32 v17, 0xffff0000, v48
	v_fmac_f32_e32 v20, v15, v16
	v_fmac_f32_e32 v21, v15, v17
	v_lshlrev_b32_e32 v16, 16, v37
	v_and_b32_e32 v17, 0xffff0000, v37
	v_mul_f32_e32 v22, v12, v16
	v_mul_f32_e32 v23, v12, v17
	v_lshlrev_b32_e32 v16, 16, v41
	v_and_b32_e32 v17, 0xffff0000, v41
	v_fmac_f32_e32 v22, v13, v16
	v_fmac_f32_e32 v23, v13, v17
	v_lshlrev_b32_e32 v16, 16, v45
	v_and_b32_e32 v17, 0xffff0000, v45
	v_fmac_f32_e32 v22, v14, v16
	v_fmac_f32_e32 v23, v14, v17
	v_lshlrev_b32_e32 v16, 16, v49
	v_and_b32_e32 v17, 0xffff0000, v49
	v_fmac_f32_e32 v22, v15, v16
	v_fmac_f32_e32 v23, v15, v17
	v_lshlrev_b32_e32 v16, 16, v38
	v_and_b32_e32 v17, 0xffff0000, v38
	v_mul_f32_e32 v24, v12, v16
	v_mul_f32_e32 v25, v12, v17
	v_lshlrev_b32_e32 v16, 16, v42
	v_and_b32_e32 v17, 0xffff0000, v42
	v_fmac_f32_e32 v24, v13, v16
	v_fmac_f32_e32 v25, v13, v17
	v_lshlrev_b32_e32 v16, 16, v46
	v_and_b32_e32 v17, 0xffff0000, v46
	v_fmac_f32_e32 v24, v14, v16
	v_fmac_f32_e32 v25, v14, v17
	v_lshlrev_b32_e32 v16, 16, v50
	v_and_b32_e32 v17, 0xffff0000, v50
	v_fmac_f32_e32 v24, v15, v16
	v_fmac_f32_e32 v25, v15, v17
	v_lshlrev_b32_e32 v16, 16, v39
	v_and_b32_e32 v17, 0xffff0000, v39
	v_mul_f32_e32 v26, v12, v16
	v_mul_f32_e32 v27, v12, v17
	v_lshlrev_b32_e32 v16, 16, v43
	v_and_b32_e32 v17, 0xffff0000, v43
	v_fmac_f32_e32 v26, v13, v16
	v_fmac_f32_e32 v27, v13, v17
	v_lshlrev_b32_e32 v16, 16, v47
	v_and_b32_e32 v17, 0xffff0000, v47
	v_fmac_f32_e32 v26, v14, v16
	v_fmac_f32_e32 v27, v14, v17
	v_lshlrev_b32_e32 v16, 16, v51
	v_and_b32_e32 v17, 0xffff0000, v51
	v_fmac_f32_e32 v26, v15, v16
	v_fmac_f32_e32 v27, v15, v17
	v_mov_b32_e32 v18, 0
	v_mov_b32_e32 v19, 0
	v_lshlrev_b32_e32 v11, 3, v190
	v_cvt_pk_fp8_f32 v18, v20, v21
	v_cvt_pk_fp8_f32 v19, v24, v25
	s_nop 0
	v_cvt_pk_fp8_f32 v18, v22, v23 op_sel:[0,0,1]
	v_cvt_pk_fp8_f32 v19, v26, v27 op_sel:[0,0,1]
	s_nop 0
	global_store_dwordx2 v11, v[18:19], s[16:17]
	v_bfe_u32 v8, v191, 15, 5
	v_cmp_lt_u32_e32 vcc, 0, v8
	s_nop 1
	v_cndmask_b32_e32 v52, v149, v52, vcc
	v_cmp_lt_u32_e32 vcc, 1, v8
	s_nop 1
	v_cndmask_b32_e32 v53, v149, v53, vcc
	v_cmp_lt_u32_e32 vcc, 2, v8
	s_nop 1
	v_cndmask_b32_e32 v54, v149, v54, vcc
	v_max3_f32 v9, v52, v53, v54
	v_max_f32_e32 v9, v9, v55
	v_sub_f32_e32 v10, v52, v9
	v_mul_f32_e32 v16, 0x3fb8aa3b, v10
	v_fma_f32 v17, v10, s94, -v16
	v_rndne_f32_e32 v18, v16
	v_fmac_f32_e32 v17, 0x32a5705f, v10
	v_sub_f32_e32 v16, v16, v18
	v_add_f32_e32 v16, v16, v17
	v_exp_f32_e32 v12, v16
	v_cvt_i32_f32_e32 v18, v18
	v_cmp_ngt_f32_e32 vcc, s95, v10
	v_ldexp_f32 v12, v12, v18
	s_nop 1
	v_cndmask_b32_e32 v12, 0, v12, vcc
	v_cmp_nlt_f32_e32 vcc, s96, v10
	s_nop 1
	v_cndmask_b32_e32 v12, v227, v12, vcc
	v_sub_f32_e32 v10, v53, v9
	v_mul_f32_e32 v16, 0x3fb8aa3b, v10
	v_fma_f32 v17, v10, s94, -v16
	v_rndne_f32_e32 v18, v16
	v_fmac_f32_e32 v17, 0x32a5705f, v10
	v_sub_f32_e32 v16, v16, v18
	v_add_f32_e32 v16, v16, v17
	v_exp_f32_e32 v13, v16
	v_cvt_i32_f32_e32 v18, v18
	v_cmp_ngt_f32_e32 vcc, s95, v10
	v_ldexp_f32 v13, v13, v18
	s_nop 1
	v_cndmask_b32_e32 v13, 0, v13, vcc
	v_cmp_nlt_f32_e32 vcc, s96, v10
	s_nop 1
	v_cndmask_b32_e32 v13, v227, v13, vcc
	v_sub_f32_e32 v10, v54, v9
	v_mul_f32_e32 v16, 0x3fb8aa3b, v10
	v_fma_f32 v17, v10, s94, -v16
	v_rndne_f32_e32 v18, v16
	v_fmac_f32_e32 v17, 0x32a5705f, v10
	v_sub_f32_e32 v16, v16, v18
	v_add_f32_e32 v16, v16, v17
	v_exp_f32_e32 v14, v16
	v_cvt_i32_f32_e32 v18, v18
	v_cmp_ngt_f32_e32 vcc, s95, v10
	v_ldexp_f32 v14, v14, v18
	s_nop 1
	v_cndmask_b32_e32 v14, 0, v14, vcc
	v_cmp_nlt_f32_e32 vcc, s96, v10
	s_nop 1
	v_cndmask_b32_e32 v14, v227, v14, vcc
	v_sub_f32_e32 v10, v55, v9
	v_mul_f32_e32 v16, 0x3fb8aa3b, v10
	v_fma_f32 v17, v10, s94, -v16
	v_rndne_f32_e32 v18, v16
	v_fmac_f32_e32 v17, 0x32a5705f, v10
	v_sub_f32_e32 v16, v16, v18
	v_add_f32_e32 v16, v16, v17
	v_exp_f32_e32 v15, v16
	v_cvt_i32_f32_e32 v18, v18
	v_cmp_ngt_f32_e32 vcc, s95, v10
	v_ldexp_f32 v15, v15, v18
	s_nop 1
	v_cndmask_b32_e32 v15, 0, v15, vcc
	v_cmp_nlt_f32_e32 vcc, s96, v10
	s_nop 1
	v_cndmask_b32_e32 v15, v227, v15, vcc
	v_add_f32_e32 v16, v12, v13
	v_add_f32_e32 v16, v14, v16
	v_add_f32_e32 v16, v15, v16
	v_div_scale_f32 v17, s[2:3], v16, v16, 1.0
	v_rcp_f32_e32 v18, v17
	s_nop 0
	v_fma_f32 v19, -v17, v18, 1.0
	v_fmac_f32_e32 v18, v19, v18
	v_div_scale_f32 v20, vcc, 1.0, v16, 1.0
	v_mul_f32_e32 v21, v20, v18
	v_fma_f32 v22, -v17, v21, v20
	v_fmac_f32_e32 v21, v22, v18
	v_fma_f32 v17, -v17, v21, v20
	v_div_fmas_f32 v17, v17, v18, v21
	v_div_fixup_f32 v16, v17, v16, 1.0
	v_mul_f32_e32 v16, 0x41800000, v16
	v_mul_f32_e32 v12, v12, v16
	v_mul_f32_e32 v13, v13, v16
	v_mul_f32_e32 v14, v14, v16
	v_mul_f32_e32 v15, v15, v16
	v_lshlrev_b32_e32 v16, 16, v56
	v_and_b32_e32 v17, 0xffff0000, v56
	v_mul_f32_e32 v20, v12, v16
	v_mul_f32_e32 v21, v12, v17
	v_lshlrev_b32_e32 v16, 16, v60
	v_and_b32_e32 v17, 0xffff0000, v60
	v_fmac_f32_e32 v20, v13, v16
	v_fmac_f32_e32 v21, v13, v17
	v_lshlrev_b32_e32 v16, 16, v192
	v_and_b32_e32 v17, 0xffff0000, v192
	v_fmac_f32_e32 v20, v14, v16
	v_fmac_f32_e32 v21, v14, v17
	v_lshlrev_b32_e32 v16, 16, v196
	v_and_b32_e32 v17, 0xffff0000, v196
	v_fmac_f32_e32 v20, v15, v16
	v_fmac_f32_e32 v21, v15, v17
	v_lshlrev_b32_e32 v16, 16, v57
	v_and_b32_e32 v17, 0xffff0000, v57
	v_mul_f32_e32 v22, v12, v16
	v_mul_f32_e32 v23, v12, v17
	v_lshlrev_b32_e32 v16, 16, v61
	v_and_b32_e32 v17, 0xffff0000, v61
	v_fmac_f32_e32 v22, v13, v16
	v_fmac_f32_e32 v23, v13, v17
	v_lshlrev_b32_e32 v16, 16, v193
	v_and_b32_e32 v17, 0xffff0000, v193
	v_fmac_f32_e32 v22, v14, v16
	v_fmac_f32_e32 v23, v14, v17
	v_lshlrev_b32_e32 v16, 16, v197
	v_and_b32_e32 v17, 0xffff0000, v197
	v_fmac_f32_e32 v22, v15, v16
	v_fmac_f32_e32 v23, v15, v17
	v_lshlrev_b32_e32 v16, 16, v58
	v_and_b32_e32 v17, 0xffff0000, v58
	v_mul_f32_e32 v24, v12, v16
	v_mul_f32_e32 v25, v12, v17
	v_lshlrev_b32_e32 v16, 16, v62
	v_and_b32_e32 v17, 0xffff0000, v62
	v_fmac_f32_e32 v24, v13, v16
	v_fmac_f32_e32 v25, v13, v17
	v_lshlrev_b32_e32 v16, 16, v194
	v_and_b32_e32 v17, 0xffff0000, v194
	v_fmac_f32_e32 v24, v14, v16
	v_fmac_f32_e32 v25, v14, v17
	v_lshlrev_b32_e32 v16, 16, v198
	v_and_b32_e32 v17, 0xffff0000, v198
	v_fmac_f32_e32 v24, v15, v16
	v_fmac_f32_e32 v25, v15, v17
	v_lshlrev_b32_e32 v16, 16, v59
	v_and_b32_e32 v17, 0xffff0000, v59
	v_mul_f32_e32 v26, v12, v16
	v_mul_f32_e32 v27, v12, v17
	v_lshlrev_b32_e32 v16, 16, v63
	v_and_b32_e32 v17, 0xffff0000, v63
	v_fmac_f32_e32 v26, v13, v16
	v_fmac_f32_e32 v27, v13, v17
	v_lshlrev_b32_e32 v16, 16, v195
	v_and_b32_e32 v17, 0xffff0000, v195
	v_fmac_f32_e32 v26, v14, v16
	v_fmac_f32_e32 v27, v14, v17
	v_lshlrev_b32_e32 v16, 16, v199
	v_and_b32_e32 v17, 0xffff0000, v199
	v_fmac_f32_e32 v26, v15, v16
	v_fmac_f32_e32 v27, v15, v17
	v_mov_b32_e32 v18, 0
	v_mov_b32_e32 v19, 0
	v_lshlrev_b32_e32 v11, 3, v191
	v_cvt_pk_fp8_f32 v18, v20, v21
	v_cvt_pk_fp8_f32 v19, v24, v25
	s_nop 0
	v_cvt_pk_fp8_f32 v18, v22, v23 op_sel:[0,0,1]
	v_cvt_pk_fp8_f32 v19, v26, v27 op_sel:[0,0,1]
	s_nop 0
	global_store_dwordx2 v11, v[18:19], s[16:17]
	v_add_u32_e32 v2, s48, v2
	s_add_u32 s49, s49, s48
	v_min_u32_e32 v190, s43, v2
	v_lshrrev_b32_e32 v9, 3, v190
	v_bfe_u32 v8, v190, 15, 5
	v_and_b32_e32 v10, 7, v190
	v_lshlrev_b32_e32 v11, 9, v9
	v_lshlrev_b32_e32 v9, 4, v9
	v_lshl_add_u32 v10, v10, 4, v11
	global_load_dwordx4 v[32:35], v9, s[14:15]
	global_load_dwordx4 v[48:51], v10, s[44:45] offset:384
	v_cmp_lt_u32_e32 vcc, 0, v8
	s_nop 1
	v_cndmask_b32_e32 v11, v150, v148, vcc
	v_add_u32_e32 v11, v11, v10
	global_load_dwordx4 v[36:39], v11, s[44:45]
	v_cmp_lt_u32_e32 vcc, 1, v8
	s_nop 1
	v_cndmask_b32_e32 v11, v150, v64, vcc
	v_add_u32_e32 v11, v11, v10
	global_load_dwordx4 v[40:43], v11, s[44:45]
	v_cmp_lt_u32_e32 vcc, 2, v8
	s_nop 1
	v_cndmask_b32_e32 v11, v150, v65, vcc
	v_add_u32_e32 v11, v11, v10
	global_load_dwordx4 v[44:47], v11, s[44:45]
	v_add_u32_e32 v191, s42, v2
	v_min_u32_e32 v191, s43, v191
	v_lshrrev_b32_e32 v9, 3, v191
	v_bfe_u32 v8, v191, 15, 5
	v_and_b32_e32 v10, 7, v191
	v_lshlrev_b32_e32 v11, 9, v9
	v_lshlrev_b32_e32 v9, 4, v9
	v_lshl_add_u32 v10, v10, 4, v11
	global_load_dwordx4 v[52:55], v9, s[14:15]
	global_load_dwordx4 v[196:199], v10, s[44:45] offset:384
	v_cmp_lt_u32_e32 vcc, 0, v8
	s_nop 1
	v_cndmask_b32_e32 v11, v150, v148, vcc
	v_add_u32_e32 v11, v11, v10
	global_load_dwordx4 v[56:59], v11, s[44:45]
	v_cmp_lt_u32_e32 vcc, 1, v8
	s_nop 1
	v_cndmask_b32_e32 v11, v150, v64, vcc
	v_add_u32_e32 v11, v11, v10
	global_load_dwordx4 v[60:63], v11, s[44:45]
	v_cmp_lt_u32_e32 vcc, 2, v8
	s_nop 1
	v_cndmask_b32_e32 v11, v150, v65, vcc
	v_add_u32_e32 v11, v11, v10
	global_load_dwordx4 v[192:195], v11, s[44:45]
	s_waitcnt vmcnt(12)
	v_bfe_u32 v8, v238, 15, 5
	v_cmp_lt_u32_e32 vcc, 0, v8
	s_nop 1
	v_cndmask_b32_e32 v200, v149, v200, vcc
	v_cmp_lt_u32_e32 vcc, 1, v8
	s_nop 1
	v_cndmask_b32_e32 v201, v149, v201, vcc
	v_cmp_lt_u32_e32 vcc, 2, v8
	s_nop 1
	v_cndmask_b32_e32 v202, v149, v202, vcc
	v_max3_f32 v9, v200, v201, v202
	v_max_f32_e32 v9, v9, v203
	v_sub_f32_e32 v10, v200, v9
	v_mul_f32_e32 v16, 0x3fb8aa3b, v10
	v_fma_f32 v17, v10, s94, -v16
	v_rndne_f32_e32 v18, v16
	v_fmac_f32_e32 v17, 0x32a5705f, v10
	v_sub_f32_e32 v16, v16, v18
	v_add_f32_e32 v16, v16, v17
	v_exp_f32_e32 v12, v16
	v_cvt_i32_f32_e32 v18, v18
	v_cmp_ngt_f32_e32 vcc, s95, v10
	v_ldexp_f32 v12, v12, v18
	s_nop 1
	v_cndmask_b32_e32 v12, 0, v12, vcc
	v_cmp_nlt_f32_e32 vcc, s96, v10
	s_nop 1
	v_cndmask_b32_e32 v12, v227, v12, vcc
	v_sub_f32_e32 v10, v201, v9
	v_mul_f32_e32 v16, 0x3fb8aa3b, v10
	v_fma_f32 v17, v10, s94, -v16
	v_rndne_f32_e32 v18, v16
	v_fmac_f32_e32 v17, 0x32a5705f, v10
	v_sub_f32_e32 v16, v16, v18
	v_add_f32_e32 v16, v16, v17
	v_exp_f32_e32 v13, v16
	v_cvt_i32_f32_e32 v18, v18
	v_cmp_ngt_f32_e32 vcc, s95, v10
	v_ldexp_f32 v13, v13, v18
	s_nop 1
	v_cndmask_b32_e32 v13, 0, v13, vcc
	v_cmp_nlt_f32_e32 vcc, s96, v10
	s_nop 1
	v_cndmask_b32_e32 v13, v227, v13, vcc
	v_sub_f32_e32 v10, v202, v9
	v_mul_f32_e32 v16, 0x3fb8aa3b, v10
	v_fma_f32 v17, v10, s94, -v16
	v_rndne_f32_e32 v18, v16
	v_fmac_f32_e32 v17, 0x32a5705f, v10
	v_sub_f32_e32 v16, v16, v18
	v_add_f32_e32 v16, v16, v17
	v_exp_f32_e32 v14, v16
	v_cvt_i32_f32_e32 v18, v18
	v_cmp_ngt_f32_e32 vcc, s95, v10
	v_ldexp_f32 v14, v14, v18
	s_nop 1
	v_cndmask_b32_e32 v14, 0, v14, vcc
	v_cmp_nlt_f32_e32 vcc, s96, v10
	s_nop 1
	v_cndmask_b32_e32 v14, v227, v14, vcc
	v_sub_f32_e32 v10, v203, v9
	v_mul_f32_e32 v16, 0x3fb8aa3b, v10
	v_fma_f32 v17, v10, s94, -v16
	v_rndne_f32_e32 v18, v16
	v_fmac_f32_e32 v17, 0x32a5705f, v10
	v_sub_f32_e32 v16, v16, v18
	v_add_f32_e32 v16, v16, v17
	v_exp_f32_e32 v15, v16
	v_cvt_i32_f32_e32 v18, v18
	v_cmp_ngt_f32_e32 vcc, s95, v10
	v_ldexp_f32 v15, v15, v18
	s_nop 1
	v_cndmask_b32_e32 v15, 0, v15, vcc
	v_cmp_nlt_f32_e32 vcc, s96, v10
	s_nop 1
	v_cndmask_b32_e32 v15, v227, v15, vcc
	v_add_f32_e32 v16, v12, v13
	v_add_f32_e32 v16, v14, v16
	v_add_f32_e32 v16, v15, v16
	v_div_scale_f32 v17, s[2:3], v16, v16, 1.0
	v_rcp_f32_e32 v18, v17
	s_nop 0
	v_fma_f32 v19, -v17, v18, 1.0
	v_fmac_f32_e32 v18, v19, v18
	v_div_scale_f32 v20, vcc, 1.0, v16, 1.0
	v_mul_f32_e32 v21, v20, v18
	v_fma_f32 v22, -v17, v21, v20
	v_fmac_f32_e32 v21, v22, v18
	v_fma_f32 v17, -v17, v21, v20
	v_div_fmas_f32 v17, v17, v18, v21
	v_div_fixup_f32 v16, v17, v16, 1.0
	v_mul_f32_e32 v16, 0x41800000, v16
	v_mul_f32_e32 v12, v12, v16
	v_mul_f32_e32 v13, v13, v16
	v_mul_f32_e32 v14, v14, v16
	v_mul_f32_e32 v15, v15, v16
	v_lshlrev_b32_e32 v16, 16, v204
	v_and_b32_e32 v17, 0xffff0000, v204
	v_mul_f32_e32 v20, v12, v16
	v_mul_f32_e32 v21, v12, v17
	v_lshlrev_b32_e32 v16, 16, v208
	v_and_b32_e32 v17, 0xffff0000, v208
	v_fmac_f32_e32 v20, v13, v16
	v_fmac_f32_e32 v21, v13, v17
	v_lshlrev_b32_e32 v16, 16, v212
	v_and_b32_e32 v17, 0xffff0000, v212
	v_fmac_f32_e32 v20, v14, v16
	v_fmac_f32_e32 v21, v14, v17
	v_lshlrev_b32_e32 v16, 16, v216
	v_and_b32_e32 v17, 0xffff0000, v216
	v_fmac_f32_e32 v20, v15, v16
	v_fmac_f32_e32 v21, v15, v17
	v_lshlrev_b32_e32 v16, 16, v205
	v_and_b32_e32 v17, 0xffff0000, v205
	v_mul_f32_e32 v22, v12, v16
	v_mul_f32_e32 v23, v12, v17
	v_lshlrev_b32_e32 v16, 16, v209
	v_and_b32_e32 v17, 0xffff0000, v209
	v_fmac_f32_e32 v22, v13, v16
	v_fmac_f32_e32 v23, v13, v17
	v_lshlrev_b32_e32 v16, 16, v213
	v_and_b32_e32 v17, 0xffff0000, v213
	v_fmac_f32_e32 v22, v14, v16
	v_fmac_f32_e32 v23, v14, v17
	v_lshlrev_b32_e32 v16, 16, v217
	v_and_b32_e32 v17, 0xffff0000, v217
	v_fmac_f32_e32 v22, v15, v16
	v_fmac_f32_e32 v23, v15, v17
	v_lshlrev_b32_e32 v16, 16, v206
	v_and_b32_e32 v17, 0xffff0000, v206
	v_mul_f32_e32 v24, v12, v16
	v_mul_f32_e32 v25, v12, v17
	v_lshlrev_b32_e32 v16, 16, v210
	v_and_b32_e32 v17, 0xffff0000, v210
	v_fmac_f32_e32 v24, v13, v16
	v_fmac_f32_e32 v25, v13, v17
	v_lshlrev_b32_e32 v16, 16, v214
	v_and_b32_e32 v17, 0xffff0000, v214
	v_fmac_f32_e32 v24, v14, v16
	v_fmac_f32_e32 v25, v14, v17
	v_lshlrev_b32_e32 v16, 16, v218
	v_and_b32_e32 v17, 0xffff0000, v218
	v_fmac_f32_e32 v24, v15, v16
	v_fmac_f32_e32 v25, v15, v17
	v_lshlrev_b32_e32 v16, 16, v207
	v_and_b32_e32 v17, 0xffff0000, v207
	v_mul_f32_e32 v26, v12, v16
	v_mul_f32_e32 v27, v12, v17
	v_lshlrev_b32_e32 v16, 16, v211
	v_and_b32_e32 v17, 0xffff0000, v211
	v_fmac_f32_e32 v26, v13, v16
	v_fmac_f32_e32 v27, v13, v17
	v_lshlrev_b32_e32 v16, 16, v215
	v_and_b32_e32 v17, 0xffff0000, v215
	v_fmac_f32_e32 v26, v14, v16
	v_fmac_f32_e32 v27, v14, v17
	v_lshlrev_b32_e32 v16, 16, v219
	v_and_b32_e32 v17, 0xffff0000, v219
	v_fmac_f32_e32 v26, v15, v16
	v_fmac_f32_e32 v27, v15, v17
	v_mov_b32_e32 v18, 0
	v_mov_b32_e32 v19, 0
	v_lshlrev_b32_e32 v11, 3, v238
	v_cvt_pk_fp8_f32 v18, v20, v21
	v_cvt_pk_fp8_f32 v19, v24, v25
	s_nop 0
	v_cvt_pk_fp8_f32 v18, v22, v23 op_sel:[0,0,1]
	v_cvt_pk_fp8_f32 v19, v26, v27 op_sel:[0,0,1]
	s_nop 0
	global_store_dwordx2 v11, v[18:19], s[16:17]
	v_bfe_u32 v8, v239, 15, 5
	v_cmp_lt_u32_e32 vcc, 0, v8
	s_nop 1
	v_cndmask_b32_e32 v240, v149, v240, vcc
	v_cmp_lt_u32_e32 vcc, 1, v8
	s_nop 1
	v_cndmask_b32_e32 v241, v149, v241, vcc
	v_cmp_lt_u32_e32 vcc, 2, v8
	s_nop 1
	v_cndmask_b32_e32 v242, v149, v242, vcc
	v_max3_f32 v9, v240, v241, v242
	v_max_f32_e32 v9, v9, v243
	v_sub_f32_e32 v10, v240, v9
	v_mul_f32_e32 v16, 0x3fb8aa3b, v10
	v_fma_f32 v17, v10, s94, -v16
	v_rndne_f32_e32 v18, v16
	v_fmac_f32_e32 v17, 0x32a5705f, v10
	v_sub_f32_e32 v16, v16, v18
	v_add_f32_e32 v16, v16, v17
	v_exp_f32_e32 v12, v16
	v_cvt_i32_f32_e32 v18, v18
	v_cmp_ngt_f32_e32 vcc, s95, v10
	v_ldexp_f32 v12, v12, v18
	s_nop 1
	v_cndmask_b32_e32 v12, 0, v12, vcc
	v_cmp_nlt_f32_e32 vcc, s96, v10
	s_nop 1
	v_cndmask_b32_e32 v12, v227, v12, vcc
	v_sub_f32_e32 v10, v241, v9
	v_mul_f32_e32 v16, 0x3fb8aa3b, v10
	v_fma_f32 v17, v10, s94, -v16
	v_rndne_f32_e32 v18, v16
	v_fmac_f32_e32 v17, 0x32a5705f, v10
	v_sub_f32_e32 v16, v16, v18
	v_add_f32_e32 v16, v16, v17
	v_exp_f32_e32 v13, v16
	v_cvt_i32_f32_e32 v18, v18
	v_cmp_ngt_f32_e32 vcc, s95, v10
	v_ldexp_f32 v13, v13, v18
	s_nop 1
	v_cndmask_b32_e32 v13, 0, v13, vcc
	v_cmp_nlt_f32_e32 vcc, s96, v10
	s_nop 1
	v_cndmask_b32_e32 v13, v227, v13, vcc
	v_sub_f32_e32 v10, v242, v9
	v_mul_f32_e32 v16, 0x3fb8aa3b, v10
	v_fma_f32 v17, v10, s94, -v16
	v_rndne_f32_e32 v18, v16
	v_fmac_f32_e32 v17, 0x32a5705f, v10
	v_sub_f32_e32 v16, v16, v18
	v_add_f32_e32 v16, v16, v17
	v_exp_f32_e32 v14, v16
	v_cvt_i32_f32_e32 v18, v18
	v_cmp_ngt_f32_e32 vcc, s95, v10
	v_ldexp_f32 v14, v14, v18
	s_nop 1
	v_cndmask_b32_e32 v14, 0, v14, vcc
	v_cmp_nlt_f32_e32 vcc, s96, v10
	s_nop 1
	v_cndmask_b32_e32 v14, v227, v14, vcc
	v_sub_f32_e32 v10, v243, v9
	v_mul_f32_e32 v16, 0x3fb8aa3b, v10
	v_fma_f32 v17, v10, s94, -v16
	v_rndne_f32_e32 v18, v16
	v_fmac_f32_e32 v17, 0x32a5705f, v10
	v_sub_f32_e32 v16, v16, v18
	v_add_f32_e32 v16, v16, v17
	v_exp_f32_e32 v15, v16
	v_cvt_i32_f32_e32 v18, v18
	v_cmp_ngt_f32_e32 vcc, s95, v10
	v_ldexp_f32 v15, v15, v18
	s_nop 1
	v_cndmask_b32_e32 v15, 0, v15, vcc
	v_cmp_nlt_f32_e32 vcc, s96, v10
	s_nop 1
	v_cndmask_b32_e32 v15, v227, v15, vcc
	v_add_f32_e32 v16, v12, v13
	v_add_f32_e32 v16, v14, v16
	v_add_f32_e32 v16, v15, v16
	v_div_scale_f32 v17, s[2:3], v16, v16, 1.0
	v_rcp_f32_e32 v18, v17
	s_nop 0
	v_fma_f32 v19, -v17, v18, 1.0
	v_fmac_f32_e32 v18, v19, v18
	v_div_scale_f32 v20, vcc, 1.0, v16, 1.0
	v_mul_f32_e32 v21, v20, v18
	v_fma_f32 v22, -v17, v21, v20
	v_fmac_f32_e32 v21, v22, v18
	v_fma_f32 v17, -v17, v21, v20
	v_div_fmas_f32 v17, v17, v18, v21
	v_div_fixup_f32 v16, v17, v16, 1.0
	v_mul_f32_e32 v16, 0x41800000, v16
	v_mul_f32_e32 v12, v12, v16
	v_mul_f32_e32 v13, v13, v16
	v_mul_f32_e32 v14, v14, v16
	v_mul_f32_e32 v15, v15, v16
	v_lshlrev_b32_e32 v16, 16, v244
	v_and_b32_e32 v17, 0xffff0000, v244
	v_mul_f32_e32 v20, v12, v16
	v_mul_f32_e32 v21, v12, v17
	v_lshlrev_b32_e32 v16, 16, v248
	v_and_b32_e32 v17, 0xffff0000, v248
	v_fmac_f32_e32 v20, v13, v16
	v_fmac_f32_e32 v21, v13, v17
	v_lshlrev_b32_e32 v16, 16, v124
	v_and_b32_e32 v17, 0xffff0000, v124
	v_fmac_f32_e32 v20, v14, v16
	v_fmac_f32_e32 v21, v14, v17
	v_lshlrev_b32_e32 v16, 16, v136
	v_and_b32_e32 v17, 0xffff0000, v136
	v_fmac_f32_e32 v20, v15, v16
	v_fmac_f32_e32 v21, v15, v17
	v_lshlrev_b32_e32 v16, 16, v245
	v_and_b32_e32 v17, 0xffff0000, v245
	v_mul_f32_e32 v22, v12, v16
	v_mul_f32_e32 v23, v12, v17
	v_lshlrev_b32_e32 v16, 16, v249
	v_and_b32_e32 v17, 0xffff0000, v249
	v_fmac_f32_e32 v22, v13, v16
	v_fmac_f32_e32 v23, v13, v17
	v_lshlrev_b32_e32 v16, 16, v125
	v_and_b32_e32 v17, 0xffff0000, v125
	v_fmac_f32_e32 v22, v14, v16
	v_fmac_f32_e32 v23, v14, v17
	v_lshlrev_b32_e32 v16, 16, v137
	v_and_b32_e32 v17, 0xffff0000, v137
	v_fmac_f32_e32 v22, v15, v16
	v_fmac_f32_e32 v23, v15, v17
	v_lshlrev_b32_e32 v16, 16, v246
	v_and_b32_e32 v17, 0xffff0000, v246
	v_mul_f32_e32 v24, v12, v16
	v_mul_f32_e32 v25, v12, v17
	v_lshlrev_b32_e32 v16, 16, v250
	v_and_b32_e32 v17, 0xffff0000, v250
	v_fmac_f32_e32 v24, v13, v16
	v_fmac_f32_e32 v25, v13, v17
	v_lshlrev_b32_e32 v16, 16, v126
	v_and_b32_e32 v17, 0xffff0000, v126
	v_fmac_f32_e32 v24, v14, v16
	v_fmac_f32_e32 v25, v14, v17
	v_lshlrev_b32_e32 v16, 16, v138
	v_and_b32_e32 v17, 0xffff0000, v138
	v_fmac_f32_e32 v24, v15, v16
	v_fmac_f32_e32 v25, v15, v17
	v_lshlrev_b32_e32 v16, 16, v247
	v_and_b32_e32 v17, 0xffff0000, v247
	v_mul_f32_e32 v26, v12, v16
	v_mul_f32_e32 v27, v12, v17
	v_lshlrev_b32_e32 v16, 16, v251
	v_and_b32_e32 v17, 0xffff0000, v251
	v_fmac_f32_e32 v26, v13, v16
	v_fmac_f32_e32 v27, v13, v17
	v_lshlrev_b32_e32 v16, 16, v127
	v_and_b32_e32 v17, 0xffff0000, v127
	v_fmac_f32_e32 v26, v14, v16
	v_fmac_f32_e32 v27, v14, v17
	v_lshlrev_b32_e32 v16, 16, v139
	v_and_b32_e32 v17, 0xffff0000, v139
	v_fmac_f32_e32 v26, v15, v16
	v_fmac_f32_e32 v27, v15, v17
	v_mov_b32_e32 v18, 0
	v_mov_b32_e32 v19, 0
	v_lshlrev_b32_e32 v11, 3, v239
	v_cvt_pk_fp8_f32 v18, v20, v21
	v_cvt_pk_fp8_f32 v19, v24, v25
	s_nop 0
	v_cvt_pk_fp8_f32 v18, v22, v23 op_sel:[0,0,1]
	v_cvt_pk_fp8_f32 v19, v26, v27 op_sel:[0,0,1]
	s_nop 0
	global_store_dwordx2 v11, v[18:19], s[16:17]
	s_cmp_le_u32 s49, s43
	s_cbranch_scc1 .Lmbm_loop
